# hyena layer-1 hosting + phase-0 idle x prefetch + batched staging loads (filter W2, hyena staging, router matrix, adaLN cond)
# baseline (speedup 1.0000x reference)
; __device__ __forceinline__ float siluf(float x) { return x / (1.0f + __expf(-x)); }
; __device__ __forceinline__ void mod_item(Frame& F, int it) {
;     ...
;     for (int i = tid; i < BATCH * DM; i += NTHR) cond[i] = siluf(c[i]);
.LBB0_19:
	global_load_dword v40, v[2:3], off
	v_lshl_add_u64 v[2:3], v[2:3], 0, s[8:9]
	global_load_dword v41, v[2:3], off
	v_lshl_add_u64 v[2:3], v[2:3], 0, s[8:9]
	global_load_dword v42, v[2:3], off
	v_lshl_add_u64 v[2:3], v[2:3], 0, s[8:9]
	global_load_dword v43, v[2:3], off
	v_lshl_add_u64 v[2:3], v[2:3], 0, s[8:9]
	global_load_dword v44, v[2:3], off
	v_lshl_add_u64 v[2:3], v[2:3], 0, s[8:9]
	global_load_dword v45, v[2:3], off
	v_lshl_add_u64 v[2:3], v[2:3], 0, s[8:9]
	global_load_dword v46, v[2:3], off
	v_lshl_add_u64 v[2:3], v[2:3], 0, s[8:9]
	global_load_dword v47, v[2:3], off
	s_waitcnt vmcnt(0)
	v_mov_b32_e32 v6, v40
	v_mul_f32_e32 v7, 0xbfb8aa3b, v6
	v_exp_f32_e32 v7, v7
	s_nop 0
	v_add_f32_e32 v7, 1.0, v7
	v_div_scale_f32 v8, s[22:23], v7, v7, v6
	v_rcp_f32_e32 v9, v8
	v_div_scale_f32 v10, vcc, v6, v7, v6
	v_fma_f32 v11, -v8, v9, 1.0
	v_fmac_f32_e32 v9, v11, v9
	v_mul_f32_e32 v11, v10, v9
	v_fma_f32 v12, -v8, v11, v10
	v_fmac_f32_e32 v11, v12, v9
	v_fma_f32 v8, -v8, v11, v10
	v_div_fmas_f32 v8, v8, v9, v11
	v_div_fixup_f32 v6, v8, v7, v6
	ds_write_b32 v4, v6
	v_mov_b32_e32 v6, v41
	v_mul_f32_e32 v7, 0xbfb8aa3b, v6
	v_exp_f32_e32 v7, v7
	s_nop 0
	v_add_f32_e32 v7, 1.0, v7
	v_div_scale_f32 v8, s[22:23], v7, v7, v6
	v_rcp_f32_e32 v9, v8
	v_div_scale_f32 v10, vcc, v6, v7, v6
	v_fma_f32 v11, -v8, v9, 1.0
	v_fmac_f32_e32 v9, v11, v9
	v_mul_f32_e32 v11, v10, v9
	v_fma_f32 v12, -v8, v11, v10
	v_fmac_f32_e32 v11, v12, v9
	v_fma_f32 v8, -v8, v11, v10
	v_div_fmas_f32 v8, v8, v9, v11
	v_div_fixup_f32 v6, v8, v7, v6
	ds_write_b32 v4, v6 offset:2048
	v_mov_b32_e32 v6, v42
	v_mul_f32_e32 v7, 0xbfb8aa3b, v6
	v_exp_f32_e32 v7, v7
	s_nop 0
	v_add_f32_e32 v7, 1.0, v7
	v_div_scale_f32 v8, s[22:23], v7, v7, v6
	v_rcp_f32_e32 v9, v8
	v_div_scale_f32 v10, vcc, v6, v7, v6
	v_fma_f32 v11, -v8, v9, 1.0
	v_fmac_f32_e32 v9, v11, v9
	v_mul_f32_e32 v11, v10, v9
	v_fma_f32 v12, -v8, v11, v10
	v_fmac_f32_e32 v11, v12, v9
	v_fma_f32 v8, -v8, v11, v10
	v_div_fmas_f32 v8, v8, v9, v11
	v_div_fixup_f32 v6, v8, v7, v6
	ds_write_b32 v4, v6 offset:4096
	v_mov_b32_e32 v6, v43
	v_mul_f32_e32 v7, 0xbfb8aa3b, v6
	v_exp_f32_e32 v7, v7
	s_nop 0
	v_add_f32_e32 v7, 1.0, v7
	v_div_scale_f32 v8, s[22:23], v7, v7, v6
	v_rcp_f32_e32 v9, v8
	v_div_scale_f32 v10, vcc, v6, v7, v6
	v_fma_f32 v11, -v8, v9, 1.0
	v_fmac_f32_e32 v9, v11, v9
	v_mul_f32_e32 v11, v10, v9
	v_fma_f32 v12, -v8, v11, v10
	v_fmac_f32_e32 v11, v12, v9
	v_fma_f32 v8, -v8, v11, v10
	v_div_fmas_f32 v8, v8, v9, v11
	v_div_fixup_f32 v6, v8, v7, v6
	ds_write_b32 v4, v6 offset:6144
	v_mov_b32_e32 v6, v44
	v_mul_f32_e32 v7, 0xbfb8aa3b, v6
	v_exp_f32_e32 v7, v7
	s_nop 0
	v_add_f32_e32 v7, 1.0, v7
	v_div_scale_f32 v8, s[22:23], v7, v7, v6
	v_rcp_f32_e32 v9, v8
	v_div_scale_f32 v10, vcc, v6, v7, v6
	v_fma_f32 v11, -v8, v9, 1.0
	v_fmac_f32_e32 v9, v11, v9
	v_mul_f32_e32 v11, v10, v9
	v_fma_f32 v12, -v8, v11, v10
	v_fmac_f32_e32 v11, v12, v9
	v_fma_f32 v8, -v8, v11, v10
	v_div_fmas_f32 v8, v8, v9, v11
	v_div_fixup_f32 v6, v8, v7, v6
	ds_write_b32 v4, v6 offset:8192
	v_mov_b32_e32 v6, v45
	v_mul_f32_e32 v7, 0xbfb8aa3b, v6
	v_exp_f32_e32 v7, v7
	s_nop 0
	v_add_f32_e32 v7, 1.0, v7
	v_div_scale_f32 v8, s[22:23], v7, v7, v6
	v_rcp_f32_e32 v9, v8
	v_div_scale_f32 v10, vcc, v6, v7, v6
	v_fma_f32 v11, -v8, v9, 1.0
	v_fmac_f32_e32 v9, v11, v9
	v_mul_f32_e32 v11, v10, v9
	v_fma_f32 v12, -v8, v11, v10
	v_fmac_f32_e32 v11, v12, v9
	v_fma_f32 v8, -v8, v11, v10
	v_div_fmas_f32 v8, v8, v9, v11
	v_div_fixup_f32 v6, v8, v7, v6
	ds_write_b32 v4, v6 offset:10240
	v_mov_b32_e32 v6, v46
	v_mul_f32_e32 v7, 0xbfb8aa3b, v6
	v_exp_f32_e32 v7, v7
	s_nop 0
	v_add_f32_e32 v7, 1.0, v7
	v_div_scale_f32 v8, s[22:23], v7, v7, v6
	v_rcp_f32_e32 v9, v8
	v_div_scale_f32 v10, vcc, v6, v7, v6
	v_fma_f32 v11, -v8, v9, 1.0
	v_fmac_f32_e32 v9, v11, v9
	v_mul_f32_e32 v11, v10, v9
	v_fma_f32 v12, -v8, v11, v10
	v_fmac_f32_e32 v11, v12, v9
	v_fma_f32 v8, -v8, v11, v10
	v_div_fmas_f32 v8, v8, v9, v11
	v_div_fixup_f32 v6, v8, v7, v6
	ds_write_b32 v4, v6 offset:12288
	v_mov_b32_e32 v6, v47
	v_mul_f32_e32 v7, 0xbfb8aa3b, v6
	v_exp_f32_e32 v7, v7
	s_nop 0
	v_add_f32_e32 v7, 1.0, v7
	v_div_scale_f32 v8, s[22:23], v7, v7, v6
	v_rcp_f32_e32 v9, v8
	v_div_scale_f32 v10, vcc, v6, v7, v6
	v_fma_f32 v11, -v8, v9, 1.0
	v_fmac_f32_e32 v9, v11, v9
	v_mul_f32_e32 v11, v10, v9
	v_fma_f32 v12, -v8, v11, v10
	v_fmac_f32_e32 v11, v12, v9
	v_fma_f32 v8, -v8, v11, v10
	v_div_fmas_f32 v8, v8, v9, v11
	v_div_fixup_f32 v6, v8, v7, v6
	ds_write_b32 v4, v6 offset:14336
